# attention DMA staging: second 1-KiB piece of each tile addressed by a second per-lane offset VGPR instead of a second scalar base (4 SALU fewer per tile)
# speedup vs baseline: 1.0171x; 1.0027x over previous
.LBB0_786:
	v_and_b32_e32 v34, 63, v171
	s_lshl_b32 s16, s0, 8
	v_and_b32_e32 v35, 0x3fffffc0, v172
	v_readlane_b32 s0, v254, 42
	v_lshlrev_b32_e32 v36, 4, v34
	v_and_b32_e32 v36, 0xc0, v36
	v_lshl_add_u32 v177, v35, 2, s0
	v_lshlrev_b32_e32 v35, 3, v34
	v_lshlrev_b32_e32 v37, 1, v34
	v_and_or_b32 v36, v35, 24, v36
	v_and_b32_e32 v37, 32, v37
	v_and_b32_e32 v35, 0x100, v35
	v_or3_b32 v192, v36, v37, v35
	s_add_i32 s1, 0, 0x400
	v_add_u32_e32 v194, s1, v192
	s_add_i32 s1, 0, 0x10400
	s_waitcnt vmcnt(4)
	s_waitcnt vmcnt(7)
	ds_write_b128 v32, v[16:19] offset:17408
	s_waitcnt vmcnt(6)
	ds_write_b128 v33, v[20:23] offset:17408
	v_add_u32_e32 v16, s1, v182
	v_exp_f32_e32 v159, v0
	v_exp_f32_e32 v161, v1
	v_exp_f32_e32 v157, v2
	v_exp_f32_e32 v160, v3
	v_exp_f32_e32 v155, v4
	v_exp_f32_e32 v158, v5
	v_exp_f32_e32 v154, v6
	v_exp_f32_e32 v156, v7
	v_exp_f32_e32 v151, v8
	v_exp_f32_e32 v153, v9
	v_exp_f32_e32 v149, v10
	v_exp_f32_e32 v152, v11
	v_exp_f32_e32 v147, v12
	v_exp_f32_e32 v150, v13
	v_exp_f32_e32 v146, v14
	v_exp_f32_e32 v148, v15
	s_waitcnt vmcnt(5)
	ds_write_b128 v16, v[24:27]
	v_add_u32_e32 v16, s1, v183
	v_mov_b32_e32 v14, v113
	v_mov_b32_e32 v15, v113
	s_waitcnt vmcnt(4)
	ds_write_b128 v16, v[28:31]
	v_cmp_gt_u32_e64 s[38:39], 32, v34
	v_mov_b32_e32 v0, v113
	v_mov_b32_e32 v1, v113
	v_mov_b32_e32 v2, v113
	v_mov_b32_e32 v3, v113
	v_mov_b32_e32 v4, v113
	v_mov_b32_e32 v5, v113
	v_mov_b32_e32 v6, v113
	v_mov_b32_e32 v7, v113
	v_mov_b32_e32 v8, v113
	v_mov_b32_e32 v9, v113
	v_mov_b32_e32 v10, v113
	v_mov_b32_e32 v11, v113
	v_mov_b32_e32 v12, v113
	v_mov_b32_e32 v13, v113
	v_mov_b64_e32 v[62:63], v[14:15]
	v_mov_b64_e32 v[46:47], v[14:15]
	v_mov_b64_e32 v[30:31], v[14:15]
	s_add_i32 s16, s16, 0x8000
	s_mov_b32 s19, 2
	s_mov_b32 s28, 4
	s_mov_b32 s0, 1
	v_lshl_add_u32 v178, v173, 2, v177
	s_mov_b32 s29, 0
	v_mov_b32_e32 v179, 0
	v_mov_b64_e32 v[60:61], v[12:13]
	v_mov_b64_e32 v[58:59], v[10:11]
	v_mov_b64_e32 v[56:57], v[8:9]
	v_mov_b64_e32 v[54:55], v[6:7]
	v_mov_b64_e32 v[52:53], v[4:5]
	v_mov_b64_e32 v[50:51], v[2:3]
	v_mov_b64_e32 v[48:49], v[0:1]
	v_mov_b64_e32 v[44:45], v[12:13]
	v_mov_b64_e32 v[42:43], v[10:11]
	v_mov_b64_e32 v[40:41], v[8:9]
	v_mov_b64_e32 v[38:39], v[6:7]
	v_mov_b64_e32 v[36:37], v[4:5]
	v_mov_b64_e32 v[34:35], v[2:3]
	v_mov_b64_e32 v[32:33], v[0:1]
	v_mov_b64_e32 v[28:29], v[12:13]
	v_mov_b64_e32 v[26:27], v[10:11]
	v_mov_b64_e32 v[24:25], v[8:9]
	v_mov_b64_e32 v[22:23], v[6:7]
	v_mov_b64_e32 v[20:21], v[4:5]
	v_mov_b64_e32 v[18:19], v[2:3]
	v_mov_b64_e32 v[16:17], v[0:1]
	s_waitcnt lgkmcnt(0)
	s_add_u32 s78, s8, s96
	s_addc_u32 s79, s9, 0
	s_add_u32 s80, s6, s96
	s_addc_u32 s81, s7, 0
	v_and_b32_e32 v183, 7, v181
	v_lshrrev_b32_e32 v185, 4, v181
	v_lshlrev_b32_e32 v185, 3, v185
	v_xor_b32_e32 v183, v183, v185
	v_and_b32_e32 v185, 15, v172
	v_xor_b32_e32 v183, v183, v185
	v_lshlrev_b32_e32 v183, 4, v183
	v_mad_u32_u24 v183, v181, s62, v183
	v_lshrrev_b32_e32 v185, 7, v172
	v_lshlrev_b32_e32 v185, 3, v185
	v_bfe_u32 v184, v172, 2, 3
	v_add_u32_e32 v185, v185, v184
	v_bfe_u32 v184, v172, 5, 2
	v_lshlrev_b32_e32 v184, 2, v184
	v_and_b32_e32 v182, 3, v172
	v_add_u32_e32 v184, v184, v182
	v_lshlrev_b32_e32 v184, 4, v184
	v_mad_u32_u24 v185, v185, s62, v184
	v_add_u32_e32 v182, 0x30000, v183
	v_add_u32_e32 v184, 0x30000, v185
	s_lshl_b32 s84, s90, 10
	s_add_i32 s65, s18, 0x80
	s_mul_i32 s65, s65, 0x1800
	s_add_u32 s66, s80, s65
	s_addc_u32 s67, s81, 0
	s_add_i32 s85, s84, 0x14400
	s_mov_b32 m0, s85
	s_nop 0
	global_load_lds_dwordx4 v183, s[66:67]
	s_add_i32 m0, s85, 0x2000
	s_nop 0
	global_load_lds_dwordx4 v182, s[66:67]
	s_barrier
.LBB0_787:
	s_mov_b32 s54, s0
	s_add_i32 s55, s28, -3
	s_lshl_b32 s21, s0, 14
	v_add_u32_e32 v180, s21, v191
	v_add_u32_e32 v84, v180, v190
	ds_read_b128 v[80:83], v84 offset:50176
	ds_read_b128 v[84:87], v84 offset:58368
	v_add_u32_e32 v195, v180, v188
	ds_read_b128 v[196:199], v195 offset:50176
	ds_read_b128 v[200:203], v195 offset:58368
	v_add_u32_e32 v195, v180, v187
	s_waitcnt lgkmcnt(3)
	v_mfma_f32_32x32x16_bf16 v[96:111], v[80:83], v[122:125], 0
	v_add_u32_e32 v180, v180, v186
	v_exp_f32_e32 v204, v72
	v_exp_f32_e32 v205, v73
	v_exp_f32_e32 v206, v74
	v_exp_f32_e32 v207, v75
	v_exp_f32_e32 v208, v76
	v_exp_f32_e32 v209, v77
	s_waitcnt lgkmcnt(2)
	v_mfma_f32_32x32x16_bf16 v[80:95], v[84:87], v[122:125], 0
	v_exp_f32_e32 v210, v78
	v_exp_f32_e32 v79, v79
	s_waitcnt lgkmcnt(1)
	v_mfma_f32_32x32x16_bf16 v[96:111], v[196:199], v[126:129], v[96:111]
	s_waitcnt lgkmcnt(0)
	v_mfma_f32_32x32x16_bf16 v[80:95], v[200:203], v[126:129], v[80:95]
	ds_read_b128 v[196:199], v195 offset:50176
	ds_read_b128 v[200:203], v195 offset:58368
	s_waitcnt lgkmcnt(1)
	v_mfma_f32_32x32x16_bf16 v[96:111], v[196:199], v[118:121], v[96:111]
	s_waitcnt lgkmcnt(0)
	v_mfma_f32_32x32x16_bf16 v[80:95], v[200:203], v[118:121], v[80:95]
	ds_read_b128 v[196:199], v180 offset:50176
	ds_read_b128 v[200:203], v180 offset:58368
	v_exp_f32_e32 v180, v64
	v_add_f32_e32 v64, v161, v159
	v_add_f32_e32 v195, v157, v160
	v_add_f32_e32 v64, v155, v64
	v_add_f32_e32 v195, v158, v195
	v_add_f32_e32 v64, v154, v64
	v_add_f32_e32 v195, v156, v195
	v_add_f32_e32 v64, v151, v64
	v_add_f32_e32 v195, v153, v195
	v_add_f32_e32 v64, v149, v64
	v_add_f32_e32 v195, v152, v195
	v_add_f32_e32 v64, v147, v64
	s_waitcnt lgkmcnt(1)
	v_mfma_f32_32x32x16_bf16 v[96:111], v[196:199], v[114:117], v[96:111]
	v_exp_f32_e32 v197, v65
	v_add_f32_e32 v195, v150, v195
	v_exp_f32_e32 v198, v66
	v_add_f32_e32 v64, v146, v64
	v_exp_f32_e32 v199, v67
	v_add_f32_e32 v195, v148, v195
	v_add_f32_e32 v64, v180, v64
	s_waitcnt lgkmcnt(0)
	v_mfma_f32_32x32x16_bf16 v[80:95], v[200:203], v[114:117], v[80:95]
	v_exp_f32_e32 v200, v68
	v_exp_f32_e32 v201, v69
	v_add_f32_e32 v195, v197, v195
	v_exp_f32_e32 v202, v70
	v_add_f32_e32 v64, v198, v64
	v_exp_f32_e32 v203, v71
	v_add_f32_e32 v195, v199, v195
	v_add_f32_e32 v64, v200, v64
	v_add_f32_e32 v195, v201, v195
	v_add_f32_e32 v64, v202, v64
	v_add_f32_e32 v195, v203, v195
	v_add_f32_e32 v64, v204, v64
	v_add_f32_e32 v195, v205, v195
	v_add_f32_e32 v64, v206, v64
	v_add_f32_e32 v195, v207, v195
	v_add_f32_e32 v64, v208, v64
	v_add_f32_e32 v195, v209, v195
	v_add_f32_e32 v64, v210, v64
	v_add_f32_e32 v195, v79, v195
	v_add_f32_e32 v195, v195, v64
	v_cvt_pk_bf16_f32 v64, v159, v161
	v_cvt_pk_bf16_f32 v65, v157, v160
	v_cvt_pk_bf16_f32 v66, v155, v158
	v_cvt_pk_bf16_f32 v67, v154, v156
	v_cvt_pk_bf16_f32 v68, v151, v153
	v_cvt_pk_bf16_f32 v69, v149, v152
	v_cvt_pk_bf16_f32 v70, v147, v150
	v_cvt_pk_bf16_f32 v71, v146, v148
	v_cvt_pk_bf16_f32 v72, v180, v197
	v_cvt_pk_bf16_f32 v73, v198, v199
	v_cvt_pk_bf16_f32 v74, v200, v201
	v_cvt_pk_bf16_f32 v75, v202, v203
	v_cvt_pk_bf16_f32 v76, v204, v205
	v_cvt_pk_bf16_f32 v77, v206, v207
	v_cvt_pk_bf16_f32 v78, v208, v209
	v_cvt_pk_bf16_f32 v79, v210, v79
	s_cmp_lt_u32 s55, 30
	s_cselect_b32 s0, 0, 0xffffffe0
	s_cselect_b32 s1, s18, s16
	s_add_i32 s0, s0, s28
	s_lshl_b32 s0, s0, 6
	s_add_i32 s0, s0, s1
	s_sub_i32 s0, s0, 64
	s_mul_i32 s64, s0, 0x1800
	s_add_u32 s66, s78, s65
	s_addc_u32 s67, s79, 0
	s_add_u32 s70, s80, s64
	s_addc_u32 s71, s81, 0
	s_lshl_b32 s85, s29, 14
	s_add_i32 s85, s85, s84
	s_add_i32 m0, s85, 0xc400
	s_nop 0
	global_load_lds_dwordx4 v183, s[70:71]
	s_add_i32 m0, s85, 0xe400
	s_nop 0
	global_load_lds_dwordx4 v182, s[70:71]
	s_lshl_b32 s85, s19, 14
	s_add_i32 s85, s85, s84
	s_add_i32 m0, s85, 0x400
	s_nop 0
	global_load_lds_dwordx4 v185, s[66:67]
	s_add_i32 m0, s85, 0x2400
	s_nop 0
	global_load_lds_dwordx4 v184, s[66:67]
	s_mov_b32 s65, s64
	s_lshl_b32 s20, s29, 14
	v_add_u32_e32 v180, s20, v194
	ds_read_b64_tr_b16 v[198:199], v180 offset:0
	ds_read_b64_tr_b16 v[200:201], v180 offset:0x800
	ds_read_b64_tr_b16 v[202:203], v180 offset:0x1000
	ds_read_b64_tr_b16 v[204:205], v180 offset:0x1800
	ds_read_b64_tr_b16 v[206:207], v180 offset:0x2000
	ds_read_b64_tr_b16 v[208:209], v180 offset:0x2800
	ds_read_b64_tr_b16 v[222:223], v180 offset:0x3000
	ds_read_b64_tr_b16 v[224:225], v180 offset:0x3800
	s_waitcnt lgkmcnt(0)
	s_nop 0
	v_mfma_f32_32x32x16_bf16 v[0:15], v[64:67], v[198:201], v[0:15]
	ds_read_b64_tr_b16 v[198:199], v180 offset:0x200
	ds_read_b64_tr_b16 v[200:201], v180 offset:0xa00
	v_mfma_f32_32x32x16_bf16 v[0:15], v[68:71], v[202:205], v[0:15]
	ds_read_b64_tr_b16 v[202:203], v180 offset:0x1200
	ds_read_b64_tr_b16 v[204:205], v180 offset:0x1a00
	v_mfma_f32_32x32x16_bf16 v[0:15], v[72:75], v[206:209], v[0:15]
	ds_read_b64_tr_b16 v[206:207], v180 offset:0x2200
	ds_read_b64_tr_b16 v[208:209], v180 offset:0x2a00
	v_mfma_f32_32x32x16_bf16 v[0:15], v[76:79], v[222:225], v[0:15]
	ds_read_b64_tr_b16 v[222:223], v180 offset:0x3200
	ds_read_b64_tr_b16 v[224:225], v180 offset:0x3a00
	s_waitcnt lgkmcnt(0)
	v_mfma_f32_32x32x16_bf16 v[48:63], v[64:67], v[198:201], v[48:63]
	ds_read_b64_tr_b16 v[198:199], v180 offset:0x400
	ds_read_b64_tr_b16 v[200:201], v180 offset:0xc00
	v_mfma_f32_32x32x16_bf16 v[48:63], v[68:71], v[202:205], v[48:63]
	ds_read_b64_tr_b16 v[202:203], v180 offset:0x1400
	ds_read_b64_tr_b16 v[204:205], v180 offset:0x1c00
	v_mfma_f32_32x32x16_bf16 v[48:63], v[72:75], v[206:209], v[48:63]
	ds_read_b64_tr_b16 v[206:207], v180 offset:0x2400
	ds_read_b64_tr_b16 v[208:209], v180 offset:0x2c00
	v_mfma_f32_32x32x16_bf16 v[48:63], v[76:79], v[222:225], v[48:63]
	ds_read_b64_tr_b16 v[222:223], v180 offset:0x3400
	ds_read_b64_tr_b16 v[224:225], v180 offset:0x3c00
	s_waitcnt lgkmcnt(0)
	v_mfma_f32_32x32x16_bf16 v[32:47], v[64:67], v[198:201], v[32:47]
	ds_read_b64_tr_b16 v[198:199], v180 offset:0x600
	ds_read_b64_tr_b16 v[200:201], v180 offset:0xe00
	v_mfma_f32_32x32x16_bf16 v[32:47], v[68:71], v[202:205], v[32:47]
	ds_read_b64_tr_b16 v[202:203], v180 offset:0x1600
	ds_read_b64_tr_b16 v[204:205], v180 offset:0x1e00
	v_mfma_f32_32x32x16_bf16 v[32:47], v[72:75], v[206:209], v[32:47]
	ds_read_b64_tr_b16 v[206:207], v180 offset:0x2600
	ds_read_b64_tr_b16 v[208:209], v180 offset:0x2e00
	v_mfma_f32_32x32x16_bf16 v[32:47], v[76:79], v[222:225], v[32:47]
	ds_read_b64_tr_b16 v[222:223], v180 offset:0x3600
	ds_read_b64_tr_b16 v[224:225], v180 offset:0x3e00
	s_waitcnt lgkmcnt(0)
	v_mfma_f32_32x32x16_bf16 v[16:31], v[64:67], v[198:201], v[16:31]
	v_max_f32_e32 v64, v96, v97
	v_max3_f32 v65, v80, v81, v82
	v_max3_f32 v64, v64, v98, v99
	v_max3_f32 v65, v65, v83, v84
	v_max3_f32 v64, v64, v100, v101
	v_mfma_f32_32x32x16_bf16 v[16:31], v[68:71], v[202:205], v[16:31]
	v_max3_f32 v65, v65, v85, v86
	v_max3_f32 v64, v64, v102, v103
	v_max3_f32 v65, v65, v87, v88
	v_max3_f32 v64, v64, v104, v105
	v_max3_f32 v65, v65, v89, v90
	v_max3_f32 v64, v64, v106, v107
	v_max3_f32 v65, v65, v91, v92
	v_mfma_f32_32x32x16_bf16 v[16:31], v[72:75], v[206:209], v[16:31]
	v_max3_f32 v64, v64, v108, v109
	v_max3_f32 v65, v65, v93, v94
	v_max3_f32 v64, v64, v110, v111
	v_max3_f32 v64, v64, v65, v95
	v_mov_b32_e32 v198, 1.0
	v_mfma_f32_32x32x16_bf16 v[16:31], v[76:79], v[222:225], v[16:31]
	v_cmp_ge_f32_e64 s[40:41], s75, v64
	s_and_b64 s[0:1], s[56:57], s[40:41]
	s_cmp_eq_u64 s[0:1], exec
	s_cbranch_scc0 .LBB0_801

.LBB0_792:
	v_exp_f32_e32 v197, v96
	v_exp_f32_e32 v208, v97
	v_exp_f32_e32 v209, v98
	v_exp_f32_e32 v210, v99
	v_exp_f32_e32 v211, v100
	v_exp_f32_e32 v220, v101
	v_exp_f32_e32 v221, v102
	v_exp_f32_e32 v222, v103
	v_exp_f32_e32 v223, v104
	v_exp_f32_e32 v224, v105
	v_exp_f32_e32 v225, v106
	v_exp_f32_e32 v226, v107
	v_exp_f32_e32 v227, v108
	v_exp_f32_e32 v228, v109
	v_exp_f32_e32 v229, v110
	v_exp_f32_e32 v230, v111
	s_waitcnt lgkmcnt(0)
	s_waitcnt vmcnt(4)
	s_barrier
	v_add_u32_e32 v199, s22, v189
	v_add_u32_e32 v68, v199, v190
	ds_read_b128 v[64:67], v68 offset:50176
	ds_read_b128 v[68:71], v68 offset:58368
	v_add_u32_e32 v204, v199, v188
	ds_read_b128 v[200:203], v204 offset:50176
	ds_read_b128 v[204:207], v204 offset:58368
	v_exp_f32_e32 v231, v87
	s_waitcnt lgkmcnt(3)
	v_mfma_f32_32x32x16_bf16 v[96:111], v[64:67], v[122:125], 0
	v_exp_f32_e32 v232, v88
	v_exp_f32_e32 v233, v89
	v_exp_f32_e32 v234, v90
	v_exp_f32_e32 v235, v91
	v_exp_f32_e32 v236, v92
	v_exp_f32_e32 v237, v93
	v_exp_f32_e32 v238, v94
	s_waitcnt lgkmcnt(2)
	v_mfma_f32_32x32x16_bf16 v[64:79], v[68:71], v[122:125], 0
	v_exp_f32_e32 v95, v95
	s_waitcnt lgkmcnt(1)
	v_mfma_f32_32x32x16_bf16 v[96:111], v[200:203], v[126:129], v[96:111]
	s_waitcnt lgkmcnt(0)
	v_mfma_f32_32x32x16_bf16 v[64:79], v[204:207], v[126:129], v[64:79]
	v_add_u32_e32 v204, v199, v187
	ds_read_b128 v[200:203], v204 offset:50176
	ds_read_b128 v[204:207], v204 offset:58368
	v_add_u32_e32 v199, v199, v186
	s_waitcnt lgkmcnt(1)
	v_mfma_f32_32x32x16_bf16 v[96:111], v[200:203], v[118:121], v[96:111]
	s_waitcnt lgkmcnt(0)
	v_mfma_f32_32x32x16_bf16 v[64:79], v[204:207], v[118:121], v[64:79]
	ds_read_b128 v[200:203], v199 offset:50176
	ds_read_b128 v[204:207], v199 offset:58368
	s_waitcnt lgkmcnt(1)
	v_mfma_f32_32x32x16_bf16 v[96:111], v[200:203], v[114:117], v[96:111]
	v_exp_f32_e32 v201, v80
	v_add_f32_e32 v80, v208, v197
	v_add_f32_e32 v199, v209, v210
	v_add_f32_e32 v80, v211, v80
	v_add_f32_e32 v199, v220, v199
	v_add_f32_e32 v80, v221, v80
	v_add_f32_e32 v199, v222, v199
	v_add_f32_e32 v80, v223, v80
	v_add_f32_e32 v199, v224, v199
	v_add_f32_e32 v80, v225, v80
	v_add_f32_e32 v199, v226, v199
	v_add_f32_e32 v80, v227, v80
	v_exp_f32_e32 v202, v81
	v_add_f32_e32 v199, v228, v199
	v_exp_f32_e32 v203, v82
	v_add_f32_e32 v80, v229, v80
	s_waitcnt lgkmcnt(0)
	v_mfma_f32_32x32x16_bf16 v[64:79], v[204:207], v[114:117], v[64:79]
	v_exp_f32_e32 v204, v83
	v_add_f32_e32 v199, v230, v199
	v_exp_f32_e32 v205, v84
	v_add_f32_e32 v80, v201, v80
	v_exp_f32_e32 v206, v85
	v_add_f32_e32 v199, v202, v199
	v_exp_f32_e32 v207, v86
	v_add_f32_e32 v80, v203, v80
	v_add_f32_e32 v199, v204, v199
	v_add_f32_e32 v80, v205, v80
	v_add_f32_e32 v199, v206, v199
	v_add_f32_e32 v80, v207, v80
	v_add_f32_e32 v199, v231, v199
	v_add_f32_e32 v80, v232, v80
	v_add_f32_e32 v199, v233, v199
	v_add_f32_e32 v80, v234, v80
	v_add_f32_e32 v199, v235, v199
	v_add_f32_e32 v80, v236, v80
	v_add_f32_e32 v199, v237, v199
	v_add_f32_e32 v80, v238, v80
	v_add_f32_e32 v199, v95, v199
	v_add_f32_e32 v199, v199, v80
	v_cvt_pk_bf16_f32 v80, v197, v208
	v_cvt_pk_bf16_f32 v81, v209, v210
	v_cvt_pk_bf16_f32 v82, v211, v220
	v_cvt_pk_bf16_f32 v83, v221, v222
	v_cvt_pk_bf16_f32 v84, v223, v224
	v_cvt_pk_bf16_f32 v85, v225, v226
	v_cvt_pk_bf16_f32 v86, v227, v228
	v_cvt_pk_bf16_f32 v87, v229, v230
	v_cvt_pk_bf16_f32 v88, v201, v202
	v_cvt_pk_bf16_f32 v89, v203, v204
	v_cvt_pk_bf16_f32 v90, v205, v206
	v_cvt_pk_bf16_f32 v91, v207, v231
	v_cvt_pk_bf16_f32 v92, v232, v233
	v_cvt_pk_bf16_f32 v93, v234, v235
	v_cvt_pk_bf16_f32 v94, v236, v237
	v_cvt_pk_bf16_f32 v95, v238, v95
	s_cmp_lt_u32 s55, 29
	s_cselect_b32 s0, 0, 0xffffffe0
	s_cselect_b32 s1, s18, s16
	s_add_i32 s0, s0, s28
	s_lshl_b32 s0, s0, 6
	s_add_i32 s0, s0, s1
	s_mul_i32 s64, s0, 0x1800
	s_add_u32 s66, s78, s65
	s_addc_u32 s67, s79, 0
	s_add_u32 s70, s80, s64
	s_addc_u32 s71, s81, 0
	s_lshl_b32 s85, s54, 14
	s_add_i32 s85, s85, s84
	s_add_i32 m0, s85, 0xc400
	s_nop 0
	global_load_lds_dwordx4 v183, s[70:71]
	s_add_i32 m0, s85, 0xe400
	s_nop 0
	global_load_lds_dwordx4 v182, s[70:71]
	s_lshl_b32 s85, s29, 14
	s_add_i32 s85, s85, s84
	s_add_i32 m0, s85, 0x400
	s_nop 0
	global_load_lds_dwordx4 v185, s[66:67]
	s_add_i32 m0, s85, 0x2400
	s_nop 0
	global_load_lds_dwordx4 v184, s[66:67]
	s_mov_b32 s65, s64
